# v010 + attention epilogue: 16 dwordx2 row-per-lane stores widened to 8 dwordx4 via v_permlane32_swap pairs (asm guide 7.3)
# speedup vs baseline: 1.0009x; 1.0009x over previous
; __device__ __forceinline__ unsigned pk2(float lo, float hi) { f32x2 v = {lo, hi}; return __builtin_bit_cast(unsigned, __builtin_convertvector(v, bf2_t)); }
; __device__ __forceinline__ float bperm(float v, int src) { return __builtin_bit_cast(float, __builtin_amdgcn_ds_bpermute(src << 2, __builtin_bit_cast(int, v))); }
; #define A2_SBAR() __builtin_amdgcn_sched_barrier(0)
; template <int OFF> __device__ __forceinline__ s16x4 a2_tr(unsigned vb) { s16x4 r; asm volatile("ds_read_b64_tr_b16 %0, %1 offset:%2" : "=&v"(r) : "v"(vb), "i"(OFF) : "memory"); return r; }
; #define A2_SBAR() __builtin_amdgcn_sched_barrier(0)
; __device__ __forceinline__ void a3_fsm(f32x16& p, float alpha, float& l_reg, bf16x8 (&pf)[2]) {
; #pragma unroll
;     for (int r = 8; r < 16; ++r) p[r] = __builtin_amdgcn_exp2f(p[r]);
;     float ps = 0.f;
; #pragma unroll
;     for (int r = 0; r < 16; ++r) ps += p[r];
;     l_reg = l_reg * alpha + ps;
; #pragma unroll
;     for (int s = 0; s < 2; ++s) { u32x4 x; x.x = pk2(p[8 * s + 0], p[8 * s + 1]); x.y = pk2(p[8 * s + 2], p[8 * s + 3]); x.z = pk2(p[8 * s + 4], p[8 * s + 5]); x.w = pk2(p[8 * s + 6], p[8 * s + 7]); pf[s] = __builtin_bit_cast(bf16x8, x); }
; }
; template <int DT, int KH> __device__ __forceinline__ void a3_pv2(f32x16& oa, f32x16& ob, unsigned vb, const bf16x8 (&pf)[2]) {
;     constexpr int B0 = DT * 512 + (2 * KH) * 4096, B1 = B0 + 512;
;     const s16x4 al0 = a2_tr<B0>(vb), ah0 = a2_tr<B0 + 2048>(vb), al1 = a2_tr<B0 + 4096>(vb), ah1 = a2_tr<B0 + 4096 + 2048>(vb);
;     const s16x4 bl0 = a2_tr<B1>(vb), bh0 = a2_tr<B1 + 2048>(vb), bl1 = a2_tr<B1 + 4096>(vb), bh1 = a2_tr<B1 + 4096 + 2048>(vb);
;     asm volatile("s_waitcnt lgkmcnt(0)" ::: "memory"); A2_SBAR();
;     ...
;     oa = __builtin_amdgcn_mfma_f32_32x32x16_bf16(A2_PK(al0, ah0), pf[0], oa, 0, 0, 0);
;     ob = __builtin_amdgcn_mfma_f32_32x32x16_bf16(A2_PK(bl0, bh0), pf[0], ob, 0, 0, 0);
;     oa = __builtin_amdgcn_mfma_f32_32x32x16_bf16(A2_PK(al1, ah1), pf[1], oa, 0, 0, 0);
;     ob = __builtin_amdgcn_mfma_f32_32x32x16_bf16(A2_PK(bl1, bh1), pf[1], ob, 0, 0, 0);
;     ...
; }
; __device__ __forceinline__ void attn_stream(Frame& F, const float* sinkl, int u_first, int u_stride, int n_lat, int u_extra) {
;     ...
;         a3_fsm(pO, alO, l_reg, pf); A3_SB();
;         a3_pv<1>(o, vb0 + ((rb + NT - 1) & 3) * A3_BUF, pf);
;         const float ltot = l_reg + bperm(l_reg, lane ^ 32), inv = 1.f / ltot;
.LBB13_565:
	v_add_f32_e32 v73, 0, v72
	v_add_f32_e32 v73, v93, v73
	v_add_f32_e32 v73, v70, v73
	v_add_f32_e32 v73, v92, v73
	v_exp_f32_e32 v67, v82
	v_add_f32_e32 v73, v68, v73
	v_exp_f32_e32 v69, v83
	v_add_f32_e32 v73, v91, v73
	v_exp_f32_e32 v71, v84
	v_add_f32_e32 v73, v66, v73
	v_exp_f32_e32 v76, v85
	v_add_f32_e32 v73, v90, v73
	v_exp_f32_e32 v77, v86
	v_add_f32_e32 v73, v67, v73
	v_exp_f32_e32 v78, v87
	v_add_f32_e32 v73, v69, v73
	v_exp_f32_e32 v79, v88
	v_add_f32_e32 v73, v71, v73
	v_exp_f32_e32 v80, v89
	v_add_f32_e32 v73, v76, v73
	v_add_f32_e32 v73, v77, v73
	s_add_i32 s58, s58, s87
	v_add_f32_e32 v73, v78, v73
	s_lshl_b32 s4, s58, 15
	v_add_f32_e32 v73, v79, v73
	s_add_i32 s4, s4, 0x18000
	v_add_f32_e32 v96, v80, v73
	s_and_b32 s4, s4, 0x18000
	v_fmac_f32_e32 v96, v163, v74
	v_cvt_pk_bf16_f32 v73, v70, v92
	v_cvt_pk_bf16_f32 v74, v68, v91
	v_cvt_pk_bf16_f32 v75, v66, v90
	v_cvt_pk_bf16_f32 v66, v67, v69
	v_cvt_pk_bf16_f32 v67, v71, v76
	v_cvt_pk_bf16_f32 v68, v77, v78
	v_add_u32_e32 v70, s4, v147
	ds_read_b64_tr_b16 v[76:77], v70 offset:0x2000
	v_cvt_pk_bf16_f32 v69, v79, v80
	ds_read_b64_tr_b16 v[78:79], v70 offset:0x2800
	ds_read_b64_tr_b16 v[80:81], v70 offset:0x3000
	ds_read_b64_tr_b16 v[82:83], v70 offset:0x3800
	ds_read_b64_tr_b16 v[84:85], v70 offset:0x2200
	ds_read_b64_tr_b16 v[86:87], v70 offset:0x2a00
	ds_read_b64_tr_b16 v[88:89], v70 offset:0x3200
	ds_read_b64_tr_b16 v[90:91], v70 offset:0x3a00
	s_waitcnt lgkmcnt(0)
	v_mov_b32_e32 v145, v98
	v_lshl_add_u64 v[94:95], s[24:25], 0, v[144:145]
	v_cvt_pk_bf16_f32 v72, v72, v93
	s_nop 1
	v_mfma_f32_32x32x16_bf16 v[50:65], v[76:79], v[72:75], v[50:65]
	ds_read_b64_tr_b16 v[76:77], v70 offset:0x2400
	ds_read_b64_tr_b16 v[78:79], v70 offset:0x2c00
	v_mfma_f32_32x32x16_bf16 v[18:33], v[84:87], v[72:75], v[18:33]
	v_mfma_f32_32x32x16_bf16 v[50:65], v[80:83], v[66:69], v[50:65]
	ds_read_b64_tr_b16 v[80:81], v70 offset:0x3400
	ds_read_b64_tr_b16 v[82:83], v70 offset:0x3c00
	ds_read_b64_tr_b16 v[84:85], v70 offset:0x2600
	ds_read_b64_tr_b16 v[86:87], v70 offset:0x2e00
	v_mfma_f32_32x32x16_bf16 v[18:33], v[88:91], v[66:69], v[18:33]
	ds_read_b64_tr_b16 v[88:89], v70 offset:0x3600
	ds_read_b64_tr_b16 v[90:91], v70 offset:0x3e00
	s_waitcnt lgkmcnt(0)
	v_mfma_f32_32x32x16_bf16 v[34:49], v[76:79], v[72:75], v[34:49]
	v_mfma_f32_32x32x16_bf16 v[2:17], v[84:87], v[72:75], v[2:17]
	v_mfma_f32_32x32x16_bf16 v[34:49], v[80:83], v[66:69], v[34:49]
	v_mfma_f32_32x32x16_bf16 v[2:17], v[88:91], v[66:69], v[2:17]
	ds_bpermute_b32 v66, v162, v96
	s_waitcnt lgkmcnt(0)
; __device__ __forceinline__ unsigned pk2(float lo, float hi) { f32x2 v = {lo, hi}; return __builtin_bit_cast(unsigned, __builtin_convertvector(v, bf2_t)); }
; template <int BIT = 0> __device__ __forceinline__ void st8w(void* p, u32x2 v) { if ((WT_STORES >> BIT) & 1) asm volatile("global_store_dwordx2 %0, %1, off sc1\n\ts_nop 1" :: "v"(p), "v"(v) : "memory"); else *(u32x2*)p = v; }
; __device__ __forceinline__ float bperm(float v, int src) { return __builtin_bit_cast(float, __builtin_amdgcn_ds_bpermute(src << 2, __builtin_bit_cast(int, v))); }
; __device__ __forceinline__ void attn_stream(Frame& F, const float* sinkl, int u_first, int u_stride, int n_lat, int u_extra) {
;     ...
;         const float ltot = l_reg + bperm(l_reg, lane ^ 32), inv = 1.f / ltot;
;         bf16* op = ATT + mq * D + hh * HD + 4 * hi;
; #pragma unroll
;         for (int dt = 0; dt < 4; ++dt)
; #pragma unroll
;             for (int rg = 0; rg < 4; ++rg) { u32x2 wv; wv.x = pk2(o[dt][4 * rg] * inv, o[dt][4 * rg + 1] * inv); wv.y = pk2(o[dt][4 * rg + 2] * inv, o[dt][4 * rg + 3] * inv);
;                 st8w<2>(op + 32 * dt + 8 * rg, wv); }
	v_add_f32_e32 v66, v96, v66
	v_div_scale_f32 v67, s[4:5], v66, v66, 1.0
	v_rcp_f32_e32 v68, v67
	s_lshl_b32 s4, s22, 7
	s_ashr_i32 s5, s4, 31
	v_fma_f32 v69, -v67, v68, 1.0
	v_fmac_f32_e32 v68, v69, v68
	v_div_scale_f32 v69, vcc, 1.0, v66, 1.0
	v_mul_f32_e32 v70, v69, v68
	v_fma_f32 v71, -v67, v70, v69
	v_fmac_f32_e32 v70, v71, v68
	v_fma_f32 v67, -v67, v70, v69
	v_div_fmas_f32 v67, v67, v68, v70
	v_lshlrev_b64 v[68:69], 11, v[94:95]
	v_div_fixup_f32 v66, v67, v66, 1.0
	v_lshl_add_u64 v[68:69], s[12:13], 0, v[68:69]
	v_lshl_add_u64 v[68:69], s[4:5], 1, v[68:69]
	v_lshlrev_b32_e32 v70, 1, v142
	v_mov_b32_e32 v71, v98
	v_lshl_add_u64 v[68:69], v[68:69], 0, v[70:71]
	v_mbcnt_lo_u32_b32 v70, -1, 0
	v_mbcnt_hi_u32_b32 v70, -1, v70
	v_and_b32_e32 v70, 32, v70
	v_lshrrev_b32_e32 v70, 2, v70
	v_mov_b32_e32 v71, v98
	v_lshl_add_u64 v[68:69], v[68:69], 0, v[70:71]
	v_pk_mul_f32 v[50:51], v[50:51], v[66:67] op_sel_hi:[1,0]
	v_pk_mul_f32 v[52:53], v[52:53], v[66:67] op_sel_hi:[1,0]
	v_pk_mul_f32 v[54:55], v[54:55], v[66:67] op_sel_hi:[1,0]
	v_pk_mul_f32 v[56:57], v[56:57], v[66:67] op_sel_hi:[1,0]
	v_cvt_pk_bf16_f32 v50, v50, v51
	v_cvt_pk_bf16_f32 v51, v52, v53
	v_cvt_pk_bf16_f32 v52, v54, v55
	v_cvt_pk_bf16_f32 v53, v56, v57
	s_nop 1
	v_permlane32_swap_b32_e32 v50, v52
	v_permlane32_swap_b32_e32 v51, v53
	global_store_dwordx4 v[68:69], v[50:53], off
	v_pk_mul_f32 v[58:59], v[58:59], v[66:67] op_sel_hi:[1,0]
	v_pk_mul_f32 v[60:61], v[60:61], v[66:67] op_sel_hi:[1,0]
	v_pk_mul_f32 v[62:63], v[62:63], v[66:67] op_sel_hi:[1,0]
	v_pk_mul_f32 v[64:65], v[64:65], v[66:67] op_sel_hi:[1,0]
	v_cvt_pk_bf16_f32 v58, v58, v59
	v_cvt_pk_bf16_f32 v59, v60, v61
	v_cvt_pk_bf16_f32 v60, v62, v63
	v_cvt_pk_bf16_f32 v61, v64, v65
	s_nop 1
	v_permlane32_swap_b32_e32 v58, v60
	v_permlane32_swap_b32_e32 v59, v61
	global_store_dwordx4 v[68:69], v[58:61], off offset:32
	v_pk_mul_f32 v[18:19], v[18:19], v[66:67] op_sel_hi:[1,0]
	v_pk_mul_f32 v[20:21], v[20:21], v[66:67] op_sel_hi:[1,0]
	v_pk_mul_f32 v[22:23], v[22:23], v[66:67] op_sel_hi:[1,0]
	v_pk_mul_f32 v[24:25], v[24:25], v[66:67] op_sel_hi:[1,0]
	v_cvt_pk_bf16_f32 v18, v18, v19
	v_cvt_pk_bf16_f32 v19, v20, v21
	v_cvt_pk_bf16_f32 v20, v22, v23
	v_cvt_pk_bf16_f32 v21, v24, v25
	s_nop 1
	v_permlane32_swap_b32_e32 v18, v20
	v_permlane32_swap_b32_e32 v19, v21
	global_store_dwordx4 v[68:69], v[18:21], off offset:64
	v_pk_mul_f32 v[26:27], v[26:27], v[66:67] op_sel_hi:[1,0]
	v_pk_mul_f32 v[28:29], v[28:29], v[66:67] op_sel_hi:[1,0]
	v_pk_mul_f32 v[30:31], v[30:31], v[66:67] op_sel_hi:[1,0]
	v_pk_mul_f32 v[32:33], v[32:33], v[66:67] op_sel_hi:[1,0]
	v_cvt_pk_bf16_f32 v26, v26, v27
	v_cvt_pk_bf16_f32 v27, v28, v29
	v_cvt_pk_bf16_f32 v28, v30, v31
	v_cvt_pk_bf16_f32 v29, v32, v33
	s_nop 1
	v_permlane32_swap_b32_e32 v26, v28
	v_permlane32_swap_b32_e32 v27, v29
	global_store_dwordx4 v[68:69], v[26:29], off offset:96
	v_pk_mul_f32 v[34:35], v[34:35], v[66:67] op_sel_hi:[1,0]
	v_pk_mul_f32 v[36:37], v[36:37], v[66:67] op_sel_hi:[1,0]
	v_pk_mul_f32 v[38:39], v[38:39], v[66:67] op_sel_hi:[1,0]
	v_pk_mul_f32 v[40:41], v[40:41], v[66:67] op_sel_hi:[1,0]
	v_cvt_pk_bf16_f32 v34, v34, v35
	v_cvt_pk_bf16_f32 v35, v36, v37
	v_cvt_pk_bf16_f32 v36, v38, v39
	v_cvt_pk_bf16_f32 v37, v40, v41
	s_nop 1
	v_permlane32_swap_b32_e32 v34, v36
	v_permlane32_swap_b32_e32 v35, v37
	global_store_dwordx4 v[68:69], v[34:37], off offset:128
	v_pk_mul_f32 v[42:43], v[42:43], v[66:67] op_sel_hi:[1,0]
	v_pk_mul_f32 v[44:45], v[44:45], v[66:67] op_sel_hi:[1,0]
	v_pk_mul_f32 v[46:47], v[46:47], v[66:67] op_sel_hi:[1,0]
	v_pk_mul_f32 v[48:49], v[48:49], v[66:67] op_sel_hi:[1,0]
	v_cvt_pk_bf16_f32 v42, v42, v43
	v_cvt_pk_bf16_f32 v43, v44, v45
	v_cvt_pk_bf16_f32 v44, v46, v47
	v_cvt_pk_bf16_f32 v45, v48, v49
	s_nop 1
	v_permlane32_swap_b32_e32 v42, v44
	v_permlane32_swap_b32_e32 v43, v45
	global_store_dwordx4 v[68:69], v[42:45], off offset:160
	v_pk_mul_f32 v[2:3], v[2:3], v[66:67] op_sel_hi:[1,0]
	v_pk_mul_f32 v[4:5], v[4:5], v[66:67] op_sel_hi:[1,0]
	v_pk_mul_f32 v[6:7], v[6:7], v[66:67] op_sel_hi:[1,0]
	v_pk_mul_f32 v[8:9], v[8:9], v[66:67] op_sel_hi:[1,0]
	v_cvt_pk_bf16_f32 v2, v2, v3
	v_cvt_pk_bf16_f32 v3, v4, v5
	v_cvt_pk_bf16_f32 v4, v6, v7
	v_cvt_pk_bf16_f32 v5, v8, v9
	s_nop 1
	v_permlane32_swap_b32_e32 v2, v4
	v_permlane32_swap_b32_e32 v3, v5
	global_store_dwordx4 v[68:69], v[2:5], off offset:192
	v_pk_mul_f32 v[10:11], v[10:11], v[66:67] op_sel_hi:[1,0]
	v_pk_mul_f32 v[12:13], v[12:13], v[66:67] op_sel_hi:[1,0]
	v_pk_mul_f32 v[14:15], v[14:15], v[66:67] op_sel_hi:[1,0]
	v_pk_mul_f32 v[16:17], v[16:17], v[66:67] op_sel_hi:[1,0]
	v_cvt_pk_bf16_f32 v10, v10, v11
	v_cvt_pk_bf16_f32 v11, v12, v13
	v_cvt_pk_bf16_f32 v12, v14, v15
	v_cvt_pk_bf16_f32 v13, v16, v17
	s_nop 1
	v_permlane32_swap_b32_e32 v10, v12
	v_permlane32_swap_b32_e32 v11, v13
	global_store_dwordx4 v[68:69], v[10:13], off offset:224
	s_and_b64 vcc, exec, s[28:29]
	s_cbranch_vccz .LBB13_516
	s_waitcnt vmcnt(0)
	s_branch .LBB13_516

; __device__ __forceinline__ int a2_crow(int r, int hi) { return (r & 3) + 8 * (r >> 2) + 4 * hi; }
; __device__ __forceinline__ void a3_psm(f32x16& p, float& m_reg, float& alpha, bool need_mask, int kd, int hi) {
;     if (need_mask) {
; #pragma unroll
;         for (int r = 0; r < 16; ++r) { const int d = kd + a2_crow(r, hi); if (d > WIN || d < -WIN) p[r] = -INFINITY; }
;     }
;     float pmax = p[0];
; #pragma unroll
;     for (int r = 1; r < 16; ++r) pmax = fmaxf(pmax, p[r]);
;     { auto rr = __builtin_amdgcn_permlane32_swap(__float_as_uint(pmax), __float_as_uint(pmax), false, false);
;       pmax = fmaxf(__uint_as_float(rr[0]), __uint_as_float(rr[1])); }
;     float mn;
;     if (__builtin_amdgcn_ballot_w64(pmax - m_reg > A2_THR) == 0ull) { mn = m_reg; alpha = 1.f; }
;     else { mn = fmaxf(m_reg, pmax); alpha = __builtin_amdgcn_exp2f((m_reg - mn) * A2_C); m_reg = mn; }
;     const float mnC = -mn * A2_C;
; #pragma unroll
;     for (int r = 0; r < 16; ++r) p[r] = fmaf(p[r], A2_C, mnC);
; #pragma unroll
;     for (int r = 0; r < 8; ++r) p[r] = __builtin_amdgcn_exp2f(p[r]);
; }
; __device__ __forceinline__ void a3_fsm(f32x16& p, float alpha, float& l_reg, bf16x8 (&pf)[2]) {
; #pragma unroll
;     for (int r = 8; r < 16; ++r) p[r] = __builtin_amdgcn_exp2f(p[r]);
;     float ps = 0.f;
; #pragma unroll
;     for (int r = 0; r < 16; ++r) ps += p[r];
;     l_reg = l_reg * alpha + ps;
; #pragma unroll
; __device__ __forceinline__ void attn_unit(Frame& F, const float* sinkl, int unit) {
;     ...
;     for (int j = 1; j < NT; ++j) {
;         if (j + 1 < NT) asm volatile("s_waitcnt vmcnt(4)" ::: "memory"); else asm volatile("s_waitcnt vmcnt(0)" ::: "memory");
;         A3_BAR();
;         if (!A3_LATEDMA && j + 2 < NT) A3_DMA(j + 2);
;         const int bc = (j & 3) * A3_BUF, bp = ((j - 1) & 3) * A3_BUF;
;         A3_SB(); a3_qk(pE, lds + bc + A3_K, qr, kbase);
;         a3_fsm(pO, alO, l_reg, pf); A3_SB();
;         if (A3_LATEDMA && j + 2 < NT) A3_DMA(j + 2);
;         a3_pv<1>(o, vb0 + bp, pf); A3_PSM(pE, alE, j, 0);
;         A3_RESC(alE);
;         A3_SB(); a3_qk(pO, lds + bc + A3_K + 8192, qr, kbase);
;         a3_fsm(pE, alE, l_reg, pf); A3_SB();
;         a3_pv<0>(o, vb0 + bc, pf); A3_PSM(pO, alO, j, 1);
;         A3_RESC(alO);
;     }
;     a3_fsm(pO, alO, l_reg, pf); A3_SB();
;     a3_pv<1>(o, vb0 + ((NT - 1) & 3) * A3_BUF, pf);
.LBB13_690:
	v_cndmask_b32_e64 v166, v134, v135, s[4:5]
	v_mul_f32_e32 v140, 0xbe0293ee, v166
	v_pk_fma_f32 v[134:135], v[74:75], s[70:71], v[140:141] op_sel_hi:[1,0,0]
	v_add_f32_e32 v74, 0, v150
	v_add_f32_e32 v74, v151, v74
	v_add_f32_e32 v75, 0, v170
	v_add_f32_e32 v74, v152, v74
	v_add_f32_e32 v75, v171, v75
	v_add_f32_e32 v74, v153, v74
	v_add_f32_e32 v75, v172, v75
	v_add_f32_e32 v74, v154, v74
	v_add_f32_e32 v75, v173, v75
	v_add_f32_e32 v74, v155, v74
	v_add_f32_e32 v75, v174, v75
	v_add_f32_e32 v74, v156, v74
	v_add_f32_e32 v75, v175, v75
	v_add_f32_e32 v74, v157, v74
	v_add_f32_e32 v75, v176, v75
	v_add_f32_e32 v74, v158, v74
	v_add_f32_e32 v75, v177, v75
	v_add_f32_e32 v74, v159, v74
	v_add_f32_e32 v75, v167, v75
	v_add_f32_e32 v74, v160, v74
	v_add_f32_e32 v75, v168, v75
	v_add_f32_e32 v74, v161, v74
	v_add_f32_e32 v75, v169, v75
	v_mov_b32_e32 v186, v140
	v_add_f32_e32 v74, v162, v74
	v_add_f32_e32 v75, v178, v75
	v_fmamk_f32 v66, v66, 0x3e0293ee, v140
	v_fmamk_f32 v67, v67, 0x3e0293ee, v140
	v_fmamk_f32 v68, v68, 0x3e0293ee, v140
	v_fmamk_f32 v69, v69, 0x3e0293ee, v140
	v_fmamk_f32 v183, v70, 0x3e0293ee, v140
	v_fmamk_f32 v184, v71, 0x3e0293ee, v140
	v_fmamk_f32 v185, v72, 0x3e0293ee, v140
	v_fmac_f32_e32 v186, 0x3e0293ee, v73
	v_add_f32_e32 v74, v163, v74
	v_add_f32_e32 v75, v179, v75
	v_exp_f32_e32 v72, v66
	v_exp_f32_e32 v73, v67
	v_exp_f32_e32 v70, v68
	v_exp_f32_e32 v71, v69
	v_exp_f32_e32 v68, v183
	v_exp_f32_e32 v69, v184
	v_exp_f32_e32 v66, v185
	v_exp_f32_e32 v67, v186
	v_add_f32_e32 v74, v164, v74
	v_add_f32_e32 v75, v180, v75
	v_add_f32_e32 v74, v165, v74
	v_add_f32_e32 v75, v181, v75
	v_fmac_f32_e32 v74, v130, v125
	v_add_f32_e32 v125, v182, v75
	s_add_i32 s30, s30, 64
	s_add_i32 s31, s31, 1
	v_pk_fma_f32 v[136:137], v[76:77], s[70:71], v[140:141] op_sel_hi:[1,0,0]
	v_pk_fma_f32 v[138:139], v[78:79], s[70:71], v[140:141] op_sel_hi:[1,0,0]
	v_pk_fma_f32 v[140:141], v[80:81], s[70:71], v[140:141] op_sel_hi:[1,0,0]
	s_cmp_lg_u32 s24, s31
	v_fmac_f32_e32 v125, v74, v132
	s_cbranch_scc1 .LBB13_672
	v_add_f32_e32 v74, 0, v72
	v_add_f32_e32 v74, v73, v74
	v_add_f32_e32 v74, v70, v74
	v_add_f32_e32 v74, v71, v74
	v_exp_f32_e32 v76, v134
	v_add_f32_e32 v74, v68, v74
	v_exp_f32_e32 v77, v135
	v_add_f32_e32 v74, v69, v74
	v_exp_f32_e32 v78, v136
	v_add_f32_e32 v74, v66, v74
	v_exp_f32_e32 v79, v137
	v_add_f32_e32 v74, v67, v74
	v_exp_f32_e32 v80, v138
	v_add_f32_e32 v74, v76, v74
	v_exp_f32_e32 v81, v139
	v_add_f32_e32 v74, v77, v74
	v_exp_f32_e32 v82, v140
	v_add_f32_e32 v74, v78, v74
	s_lshl_b32 s4, s24, 15
	v_exp_f32_e32 v83, v141
	v_add_f32_e32 v74, v79, v74
	s_add_i32 s4, s4, 0x18000
	v_add_f32_e32 v74, v80, v74
	s_and_b32 s4, s4, 0x18000
	v_add_f32_e32 v74, v81, v74
	v_cvt_pk_bf16_f32 v72, v72, v73
	v_cvt_pk_bf16_f32 v73, v70, v71
	v_cvt_pk_bf16_f32 v75, v66, v67
	v_cvt_pk_bf16_f32 v66, v76, v77
	v_add_u32_e32 v70, s4, v131
	ds_read_b64_tr_b16 v[76:77], v70 offset:0x2000
	v_add_f32_e32 v74, v82, v74
	v_cvt_pk_bf16_f32 v67, v78, v79
	ds_read_b64_tr_b16 v[78:79], v70 offset:0x2800
	v_add_f32_e32 v92, v83, v74
	v_cvt_pk_bf16_f32 v74, v68, v69
	v_cvt_pk_bf16_f32 v68, v80, v81
	ds_read_b64_tr_b16 v[80:81], v70 offset:0x3000
	v_cvt_pk_bf16_f32 v69, v82, v83
	ds_read_b64_tr_b16 v[82:83], v70 offset:0x3800
	ds_read_b64_tr_b16 v[84:85], v70 offset:0x2200
	ds_read_b64_tr_b16 v[86:87], v70 offset:0x2a00
	ds_read_b64_tr_b16 v[88:89], v70 offset:0x3200
	ds_read_b64_tr_b16 v[90:91], v70 offset:0x3a00
	s_waitcnt lgkmcnt(0)
	v_fmac_f32_e32 v92, v125, v142
	v_mfma_f32_32x32x16_bf16 v[50:65], v[76:79], v[72:75], v[50:65]
	ds_read_b64_tr_b16 v[76:77], v70 offset:0x2400
	ds_read_b64_tr_b16 v[78:79], v70 offset:0x2c00
	v_mfma_f32_32x32x16_bf16 v[18:33], v[84:87], v[72:75], v[18:33]
	v_mfma_f32_32x32x16_bf16 v[50:65], v[80:83], v[66:69], v[50:65]
	ds_read_b64_tr_b16 v[80:81], v70 offset:0x3400
	ds_read_b64_tr_b16 v[82:83], v70 offset:0x3c00
	ds_read_b64_tr_b16 v[84:85], v70 offset:0x2600
	ds_read_b64_tr_b16 v[86:87], v70 offset:0x2e00
	v_mfma_f32_32x32x16_bf16 v[18:33], v[88:91], v[66:69], v[18:33]
	ds_read_b64_tr_b16 v[88:89], v70 offset:0x3600
	ds_read_b64_tr_b16 v[90:91], v70 offset:0x3e00
	s_waitcnt lgkmcnt(0)
	v_mfma_f32_32x32x16_bf16 v[34:49], v[76:79], v[72:75], v[34:49]
	v_mov_b32_e32 v127, v98
	s_add_i32 s12, s12, s2
	s_cmpk_lt_i32 s12, 0x210
	v_mfma_f32_32x32x16_bf16 v[2:17], v[84:87], v[72:75], v[2:17]
	v_mfma_f32_32x32x16_bf16 v[34:49], v[80:83], v[66:69], v[34:49]
	v_mfma_f32_32x32x16_bf16 v[2:17], v[88:91], v[66:69], v[2:17]
	ds_bpermute_b32 v66, v148, v92
	s_waitcnt lgkmcnt(0)
; __device__ __forceinline__ unsigned pk2(float lo, float hi) { f32x2 v = {lo, hi}; return __builtin_bit_cast(unsigned, __builtin_convertvector(v, bf2_t)); }
; template <int BIT = 0> __device__ __forceinline__ void st8w(void* p, u32x2 v) { if ((WT_STORES >> BIT) & 1) asm volatile("global_store_dwordx2 %0, %1, off sc1\n\ts_nop 1" :: "v"(p), "v"(v) : "memory"); else *(u32x2*)p = v; }
; __device__ __forceinline__ float bperm(float v, int src) { return __builtin_bit_cast(float, __builtin_amdgcn_ds_bpermute(src << 2, __builtin_bit_cast(int, v))); }
; __device__ __forceinline__ void attn_unit(Frame& F, const float* sinkl, int unit) {
;     ...
;     const float ltot = l_reg + bperm(l_reg, lane ^ 32), inv = 1.f / ltot;
;     bf16* op = ATT + mq * D + hh * HD + 4 * hi;
; #pragma unroll
;     for (int dt = 0; dt < 4; ++dt)
; #pragma unroll
;         for (int rg = 0; rg < 4; ++rg) { u32x2 wv; wv.x = pk2(o[dt][4 * rg] * inv, o[dt][4 * rg + 1] * inv); wv.y = pk2(o[dt][4 * rg + 2] * inv, o[dt][4 * rg + 3] * inv);
;             st8w<2>(op + 32 * dt + 8 * rg, wv); }
	v_add_f32_e32 v66, v92, v66
	v_div_scale_f32 v67, s[4:5], v66, v66, 1.0
	v_rcp_f32_e32 v68, v67
	s_nop 0
	v_fma_f32 v69, -v67, v68, 1.0
	v_fmac_f32_e32 v68, v69, v68
	v_div_scale_f32 v69, vcc, 1.0, v66, 1.0
	v_mul_f32_e32 v70, v69, v68
	v_fma_f32 v71, -v67, v70, v69
	v_fmac_f32_e32 v70, v71, v68
	v_fma_f32 v67, -v67, v70, v69
	v_div_fmas_f32 v67, v67, v68, v70
	v_lshlrev_b64 v[68:69], 11, v[128:129]
	v_div_fixup_f32 v66, v67, v66, 1.0
	v_lshl_add_u64 v[68:69], s[8:9], 0, v[68:69]
	v_lshl_add_u64 v[68:69], s[10:11], 1, v[68:69]
	v_lshl_add_u64 v[68:69], v[68:69], 0, v[126:127]
	v_mbcnt_lo_u32_b32 v70, -1, 0
	v_mbcnt_hi_u32_b32 v70, -1, v70
	v_and_b32_e32 v70, 32, v70
	v_lshrrev_b32_e32 v70, 2, v70
	v_mov_b32_e32 v71, v98
	v_lshl_add_u64 v[68:69], v[68:69], 0, v[70:71]
	v_pk_mul_f32 v[50:51], v[50:51], v[66:67] op_sel_hi:[1,0]
	v_pk_mul_f32 v[52:53], v[52:53], v[66:67] op_sel_hi:[1,0]
	v_pk_mul_f32 v[54:55], v[54:55], v[66:67] op_sel_hi:[1,0]
	v_pk_mul_f32 v[56:57], v[56:57], v[66:67] op_sel_hi:[1,0]
	v_cvt_pk_bf16_f32 v50, v50, v51
	v_cvt_pk_bf16_f32 v51, v52, v53
	v_cvt_pk_bf16_f32 v52, v54, v55
	v_cvt_pk_bf16_f32 v53, v56, v57
	s_nop 1
	v_permlane32_swap_b32_e32 v50, v52
	v_permlane32_swap_b32_e32 v51, v53
	global_store_dwordx4 v[68:69], v[50:53], off
	v_pk_mul_f32 v[58:59], v[58:59], v[66:67] op_sel_hi:[1,0]
	v_pk_mul_f32 v[60:61], v[60:61], v[66:67] op_sel_hi:[1,0]
	v_pk_mul_f32 v[62:63], v[62:63], v[66:67] op_sel_hi:[1,0]
	v_pk_mul_f32 v[64:65], v[64:65], v[66:67] op_sel_hi:[1,0]
	v_cvt_pk_bf16_f32 v58, v58, v59
	v_cvt_pk_bf16_f32 v59, v60, v61
	v_cvt_pk_bf16_f32 v60, v62, v63
	v_cvt_pk_bf16_f32 v61, v64, v65
	s_nop 1
	v_permlane32_swap_b32_e32 v58, v60
	v_permlane32_swap_b32_e32 v59, v61
	global_store_dwordx4 v[68:69], v[58:61], off offset:32
	v_pk_mul_f32 v[18:19], v[18:19], v[66:67] op_sel_hi:[1,0]
	v_pk_mul_f32 v[20:21], v[20:21], v[66:67] op_sel_hi:[1,0]
	v_pk_mul_f32 v[22:23], v[22:23], v[66:67] op_sel_hi:[1,0]
	v_pk_mul_f32 v[24:25], v[24:25], v[66:67] op_sel_hi:[1,0]
	v_cvt_pk_bf16_f32 v18, v18, v19
	v_cvt_pk_bf16_f32 v19, v20, v21
	v_cvt_pk_bf16_f32 v20, v22, v23
	v_cvt_pk_bf16_f32 v21, v24, v25
	s_nop 1
	v_permlane32_swap_b32_e32 v18, v20
	v_permlane32_swap_b32_e32 v19, v21
	global_store_dwordx4 v[68:69], v[18:21], off offset:64
	v_pk_mul_f32 v[26:27], v[26:27], v[66:67] op_sel_hi:[1,0]
	v_pk_mul_f32 v[28:29], v[28:29], v[66:67] op_sel_hi:[1,0]
	v_pk_mul_f32 v[30:31], v[30:31], v[66:67] op_sel_hi:[1,0]
	v_pk_mul_f32 v[32:33], v[32:33], v[66:67] op_sel_hi:[1,0]
	v_cvt_pk_bf16_f32 v26, v26, v27
	v_cvt_pk_bf16_f32 v27, v28, v29
	v_cvt_pk_bf16_f32 v28, v30, v31
	v_cvt_pk_bf16_f32 v29, v32, v33
	s_nop 1
	v_permlane32_swap_b32_e32 v26, v28
	v_permlane32_swap_b32_e32 v27, v29
	global_store_dwordx4 v[68:69], v[26:29], off offset:96
	v_pk_mul_f32 v[34:35], v[34:35], v[66:67] op_sel_hi:[1,0]
	v_pk_mul_f32 v[36:37], v[36:37], v[66:67] op_sel_hi:[1,0]
	v_pk_mul_f32 v[38:39], v[38:39], v[66:67] op_sel_hi:[1,0]
	v_pk_mul_f32 v[40:41], v[40:41], v[66:67] op_sel_hi:[1,0]
	v_cvt_pk_bf16_f32 v34, v34, v35
	v_cvt_pk_bf16_f32 v35, v36, v37
	v_cvt_pk_bf16_f32 v36, v38, v39
	v_cvt_pk_bf16_f32 v37, v40, v41
	s_nop 1
	v_permlane32_swap_b32_e32 v34, v36
	v_permlane32_swap_b32_e32 v35, v37
	global_store_dwordx4 v[68:69], v[34:37], off offset:128
	v_pk_mul_f32 v[42:43], v[42:43], v[66:67] op_sel_hi:[1,0]
	v_pk_mul_f32 v[44:45], v[44:45], v[66:67] op_sel_hi:[1,0]
	v_pk_mul_f32 v[46:47], v[46:47], v[66:67] op_sel_hi:[1,0]
	v_pk_mul_f32 v[48:49], v[48:49], v[66:67] op_sel_hi:[1,0]
	v_cvt_pk_bf16_f32 v42, v42, v43
	v_cvt_pk_bf16_f32 v43, v44, v45
	v_cvt_pk_bf16_f32 v44, v46, v47
	v_cvt_pk_bf16_f32 v45, v48, v49
	s_nop 1
	v_permlane32_swap_b32_e32 v42, v44
	v_permlane32_swap_b32_e32 v43, v45
	global_store_dwordx4 v[68:69], v[42:45], off offset:160
	v_pk_mul_f32 v[2:3], v[2:3], v[66:67] op_sel_hi:[1,0]
	v_pk_mul_f32 v[4:5], v[4:5], v[66:67] op_sel_hi:[1,0]
	v_pk_mul_f32 v[6:7], v[6:7], v[66:67] op_sel_hi:[1,0]
	v_pk_mul_f32 v[8:9], v[8:9], v[66:67] op_sel_hi:[1,0]
	v_cvt_pk_bf16_f32 v2, v2, v3
	v_cvt_pk_bf16_f32 v3, v4, v5
	v_cvt_pk_bf16_f32 v4, v6, v7
	v_cvt_pk_bf16_f32 v5, v8, v9
	s_nop 1
	v_permlane32_swap_b32_e32 v2, v4
	v_permlane32_swap_b32_e32 v3, v5
	global_store_dwordx4 v[68:69], v[2:5], off offset:192
	v_pk_mul_f32 v[10:11], v[10:11], v[66:67] op_sel_hi:[1,0]
	v_pk_mul_f32 v[12:13], v[12:13], v[66:67] op_sel_hi:[1,0]
	v_pk_mul_f32 v[14:15], v[14:15], v[66:67] op_sel_hi:[1,0]
	v_pk_mul_f32 v[16:17], v[16:17], v[66:67] op_sel_hi:[1,0]
	v_cvt_pk_bf16_f32 v10, v10, v11
	v_cvt_pk_bf16_f32 v11, v12, v13
	v_cvt_pk_bf16_f32 v12, v14, v15
	v_cvt_pk_bf16_f32 v13, v16, v17
	s_nop 1
	v_permlane32_swap_b32_e32 v10, v12
	v_permlane32_swap_b32_e32 v11, v13
	global_store_dwordx4 v[68:69], v[10:13], off offset:224
	s_cbranch_scc1 .LBB13_655
